# chunk items: L2 prefetch of the next item's raw q/k/v rows (one dword per 128-byte line, discarded) issued after step 0
# speedup vs baseline: 1.0023x; 1.0023x over previous
; __device__ __forceinline__ void gdn_local_item(const Params& P, LAS unsigned char* lds, int item, int tid, bool defer, int& pend, unsigned& pend_fb) {
;     ...
;         for (int r = 0; r < 7; ++r) {
;             const int id = tid + 512 * r;
;             const int row = id / 48, rem = id - row * 48, part = rem >> 4, ck = rem & 15, s = n * 64 + row - 3;
;             pr[r] = (v4u){0u, 0u, 0u, 0u};
;             if (id < 67 * 48 && s >= 0) pr[r] = *(const v4u*)(QKV + (size_t)(b * SEQ + s) * 1536 + part * 512 + h * 128 + ck * 8);
;     ...
;         const int c = tid >> 3, grp = tid & 7;
.LBB0_517:
	v_ashrrev_i32_e32 v92, 3, v91
	v_and_b32_e32 v46, 7, v91
	s_movk_i32 s0, 0x300
	v_lshlrev_b32_e32 v51, 6, v46
	v_lshlrev_b32_e32 v52, 5, v46
	s_waitcnt vmcnt(0)
	s_mul_i32 s98, s58, 0xe0
	v_readlane_b32 s99, v255, 10
	s_add_i32 s98, s98, s99
	s_addk_i32 s98, 0xe0
	s_lshr_b32 s99, s98, 3
	s_cmpk_gt_u32 s99, 0x7f
	s_cbranch_scc1 .Lpf_skipA
	s_and_b32 s98, s98, 7
	s_lshr_b32 s100, s98, 2
	s_and_b32 s98, s98, 3
	s_lshl_b32 s100, s100, 13
	s_lshl_b32 s99, s99, 6
	s_add_i32 s99, s99, s100
	s_add_i32 s99, s99, -3
	s_mul_i32 s99, s99, 0xc00
	s_lshl_b32 s98, s98, 8
	s_add_u32 s98, s99, s98
	s_add_u32 s100, s24, 0x3c00000
	s_addc_u32 s101, s25, 0
	s_add_u32 s100, s100, s98
	s_addc_u32 s101, s101, 0
	s_mov_b32 s98, 0x2aaaaaab
	v_mul_hi_u32 v250, v0, s98
	v_mul_u32_u24_e32 v251, 6, v250
	v_sub_u32_e32 v251, v0, v251
	v_lshrrev_b32_e32 v252, 1, v251
	v_and_b32_e32 v251, 1, v251
	v_mul_u32_u24_e32 v250, 0xc00, v250
	v_lshl_add_u32 v250, v252, 10, v250
	v_lshl_add_u32 v250, v251, 7, v250
	v_mov_b32_e32 v251, 0x192
	v_cmp_gt_u32_e64 s[98:99], v251, v0
	s_mov_b64 exec, s[98:99]
	global_load_dword v253, v250, s[100:101]
	s_mov_b64 exec, -1
.Lpf_skipA:
	v_mul_lo_u32 v4, v92, s0
	v_mul_lo_u32 v50, v92, s72
	v_mul_lo_u32 v47, v92, s73
	v_or_b32_e32 v53, v4, v52
	s_mov_b32 s12, 0
	v_mov_b32_e32 v54, v51
	s_branch .LBB0_519

; __device__ __forceinline__ void gdn_local_item(const Params& P, LAS unsigned char* lds, int item, int tid, bool defer, int& pend, unsigned& pend_fb) {
;     ...
;         for (int r = 0; r < 7; ++r) {
;             const int id = tid + 512 * r;
;             const int row = id / 48, rem = id - row * 48, part = rem >> 4, ck = rem & 15, s = n * 64 + row - 3;
;             pr[r] = (v4u){0u, 0u, 0u, 0u};
;             if (id < 67 * 48 && s >= 0) pr[r] = *(const v4u*)(QKV + (size_t)(b * SEQ + s) * 1536 + part * 512 + h * 128 + ck * 8);
; __global__ void __launch_bounds__(NWAVES * 64, 2) hybrid_fwd(Params P) {
;     ...
;                   if (wk < 192) { const int q = 672 + wk; gdn_local_item(P, lds, (q & 7) * 128 + (q >> 3), tid, true, pend, pend_fb); }
;                   if (wk < 160) { const int q = 864 + wk; gdn_local_item(P, lds, (q & 7) * 128 + (q >> 3), tid, true, pend, pend_fb); }
.LBB0_803:
	s_or_b64 exec, exec, s[0:1]
	v_ashrrev_i32_e32 v85, 3, v84
	s_movk_i32 s0, 0x210
	v_mul_lo_u32 v1, v85, s0
	s_movk_i32 s0, 0x110
	v_and_b32_e32 v45, 7, v84
	v_mul_lo_u32 v46, v85, s0
	s_movk_i32 s0, 0x300
	v_lshlrev_b32_e32 v49, 6, v45
	v_lshlrev_b32_e32 v50, 5, v45
	s_waitcnt vmcnt(0)
	v_readlane_b32 s98, v255, 10
	s_addk_i32 s98, 0x360
	s_lshr_b32 s99, s98, 3
	s_cmpk_gt_u32 s99, 0x7f
	s_cbranch_scc1 .Lpf_skipB
	s_and_b32 s98, s98, 7
	s_lshr_b32 s100, s98, 2
	s_and_b32 s98, s98, 3
	s_lshl_b32 s100, s100, 13
	s_lshl_b32 s99, s99, 6
	s_add_i32 s99, s99, s100
	s_add_i32 s99, s99, -3
	s_mul_i32 s99, s99, 0xc00
	s_lshl_b32 s98, s98, 8
	s_add_u32 s98, s99, s98
	s_add_u32 s100, s24, 0x3c00000
	s_addc_u32 s101, s25, 0
	s_add_u32 s100, s100, s98
	s_addc_u32 s101, s101, 0
	s_mov_b32 s98, 0x2aaaaaab
	v_mul_hi_u32 v250, v0, s98
	v_mul_u32_u24_e32 v251, 6, v250
	v_sub_u32_e32 v251, v0, v251
	v_lshrrev_b32_e32 v252, 1, v251
	v_and_b32_e32 v251, 1, v251
	v_mul_u32_u24_e32 v250, 0xc00, v250
	v_lshl_add_u32 v250, v252, 10, v250
	v_lshl_add_u32 v250, v251, 7, v250
	v_mov_b32_e32 v251, 0x192
	v_cmp_gt_u32_e64 s[98:99], v251, v0
	s_mov_b64 exec, s[98:99]
	global_load_dword v253, v250, s[100:101]
	s_mov_b64 exec, -1
.Lpf_skipB:
	v_mul_lo_u32 v2, v85, s0
	v_or_b32_e32 v51, v2, v50
	s_mov_b32 s13, 0xffff0000
	s_movk_i32 s14, 0x7fff
	v_mov_b32_e32 v52, 0x3db504f3
	v_mov_b32_e32 v53, v49
	s_branch .LBB0_805
